# v93: R1 router-weight loads above barrier wait (wave 0 issues them after its arrival atomic) + final-phase preamble loads overlapped
# speedup vs baseline: 1.0008x; 1.0008x over previous
; __device__ __forceinline__ unsigned xb_add(unsigned* p, unsigned v) { return __hip_atomic_fetch_add(p, v, __ATOMIC_RELAXED, __HIP_MEMORY_SCOPE_AGENT); }
; __device__ __forceinline__ void xcd_barrier(const XcdBarrier& b) {
;     ...
;         unsigned nloc = b.st[0], nx = b.st[1];
;         if (nloc == 0u) { xcd_barrier_complete(bar, b.x, nloc, nx); b.st[0] = nloc; b.st[1] = nx; }
;         const unsigned old = xb_add(&bar[XB_XSUB(b.x)], 1u);
;         const unsigned gen = old / nloc;
;         if (old + 1u == (gen + 1u) * nloc) {
; template <int layer> __device__ __forceinline__ void layer_phases(const Ctx& c, unsigned char* lds) {
;     ...
;                 { f32x4 ra[2][2]; float gk[2];
; #pragma unroll
;                   for (int j = 0; j < 2; ++j) { const int k = tid + NTHR * j; ra[j][0] = *(const f32x4*)(args.moe_router + k * 8); ra[j][1] = *(const f32x4*)(args.moe_router + k * 8 + 4); gk[j] = gf[k]; }
.LBB0_1366:
	s_or_b64 exec, exec, s[10:11]
	buffer_inv sc1
	s_mov_b64 s[98:99], exec
	s_mov_b64 exec, s[0:1]
	v_lshlrev_b32_e32 v96, 5, v0
	v_lshlrev_b32_e32 v97, 2, v0
	v_add_u32_e32 v98, 0x4000, v96
	v_add_u32_e32 v97, 0x1000, v97
	global_load_dwordx4 v[100:103], v96, s[50:51]
	global_load_dwordx4 v[104:107], v96, s[50:51] offset:16
	global_load_dword v108, v97, s[42:43]
	global_load_dword v109, v97, s[42:43] offset:2048
	global_load_dwordx4 v[110:113], v98, s[50:51]
	global_load_dwordx4 v[114:117], v98, s[50:51] offset:16
	s_mov_b64 exec, s[98:99]
	v_cvt_f32_u32_e32 v5, v3
	s_waitcnt vmcnt(7)
	v_readfirstlane_b32 s2, v4
	v_sub_u32_e32 v4, 0, v3
	v_rcp_iflag_f32_e32 v5, v5
	v_add_u32_e32 v6, s2, v2
	v_mul_f32_e32 v5, 0x4f7ffffe, v5
	v_cvt_u32_f32_e32 v5, v5
	v_mul_lo_u32 v2, v4, v5
	v_mul_hi_u32 v2, v5, v2
	v_add_u32_e32 v2, v5, v2
	v_mul_hi_u32 v2, v6, v2
	v_mul_lo_u32 v4, v2, v3
	v_sub_u32_e32 v4, v6, v4
	v_add_u32_e32 v5, 1, v2
	v_cmp_ge_u32_e32 vcc, v4, v3
	s_nop 1
	v_cndmask_b32_e32 v2, v2, v5, vcc
	v_sub_u32_e32 v5, v4, v3
	v_cndmask_b32_e32 v4, v4, v5, vcc
	v_add_u32_e32 v5, 1, v2
	v_cmp_ge_u32_e32 vcc, v4, v3
	v_add_u32_e32 v4, 1, v6
	s_nop 0
	v_cndmask_b32_e32 v2, v2, v5, vcc
	v_mul_lo_u32 v5, v3, v2
	v_add_u32_e32 v3, v5, v3
	v_cmp_ne_u32_e32 vcc, v4, v3
	s_and_saveexec_b64 s[2:3], vcc
	s_xor_b64 s[8:9], exec, s[2:3]
	s_cbranch_execz .LBB0_1380
	s_waitcnt lgkmcnt(0)
	v_mov_b32_e32 v1, 0x2000
	global_load_dword v1, v1, s[6:7] offset:1024 sc1
	s_add_u32 s12, s6, 0x2400
	s_addc_u32 s13, s7, 0
	s_waitcnt vmcnt(0)
	v_cmp_eq_u32_e32 vcc, v1, v2
	s_and_saveexec_b64 s[10:11], vcc
	s_cbranch_execz .LBB0_1379
	s_mov_b32 s2, 1
	s_mov_b64 s[14:15], 0
	v_mov_b32_e32 v1, 0
	s_branch .LBB0_1370

; __device__ __forceinline__ void xcd_barrier(const XcdBarrier& b) {
;     ...
;     __syncthreads();
; template <int layer> __device__ __forceinline__ void layer_phases(const Ctx& c, unsigned char* lds) {
;     ...
;                 { f32x4 ra[2][2]; float gk[2];
; #pragma unroll
;                   for (int j = 0; j < 2; ++j) { const int k = tid + NTHR * j; ra[j][0] = *(const f32x4*)(args.moe_router + k * 8); ra[j][1] = *(const f32x4*)(args.moe_router + k * 8 + 4); gk[j] = gf[k]; }
.Lr1_w17:
	s_or_b64 exec, exec, s[0:1]
	v_lshlrev_b32_e32 v96, 5, v0
	v_lshlrev_b32_e32 v97, 2, v0
	v_add_u32_e32 v98, 0x4000, v96
	v_add_u32_e32 v97, 0x1000, v97
	global_load_dwordx4 v[100:103], v96, s[50:51]
	global_load_dwordx4 v[104:107], v96, s[50:51] offset:16
	global_load_dword v108, v97, s[42:43]
	global_load_dword v109, v97, s[42:43] offset:2048
	global_load_dwordx4 v[110:113], v98, s[50:51]
	global_load_dwordx4 v[114:117], v98, s[50:51] offset:16
	s_branch .LBB0_1400
